# baseline (speedup 1.0000x reference)
_Z11lstm_kernelPKiPKhPKfS4_S4_Pf:
	s_load_dwordx4 s[12:15], s[0:1], 0x0
	v_readfirstlane_b32 s19, v0
	v_or_b32_e32 v3, 0x400, v0
	s_movk_i32 s4, 0x500
	s_lshr_b32 s7, s19, 6
	s_lshl_b32 s18, s2, 6
	s_mulk_i32 s2, 0x1400
	v_mov_b32_e32 v2, 0x4ff
	v_cmp_gt_u32_e32 vcc, s4, v3
	s_mul_hi_i32 s3, s18, 0x50
	s_waitcnt lgkmcnt(0)
	s_add_u32 s2, s12, s2
	v_cndmask_b32_e32 v2, v2, v3, vcc
	s_addc_u32 s3, s13, s3
	v_lshlrev_b32_e32 v1, 2, v0
	v_lshlrev_b32_e32 v4, 2, v2
	s_movk_i32 s4, 0x184
	v_or_b32_e32 v28, 0x200, v0
	global_load_dword v29, v1, s[2:3]
	global_load_dword v30, v1, s[2:3] offset:2048
	global_load_dword v2, v4, s[2:3]
	v_mov_b32_e32 v4, 0x383
	v_cmp_gt_u32_e32 vcc, s4, v0
	s_add_u32 s2, s14, 0x34000
	s_addc_u32 s3, s15, 0
	v_cndmask_b32_e32 v4, v4, v28, vcc
	v_lshlrev_b32_e32 v31, 4, v0
	v_lshlrev_b32_e32 v4, 4, v4
	global_load_dwordx4 v[6:9], v31, s[2:3]
	global_load_dwordx4 v[10:13], v4, s[2:3]
	v_and_b32_e32 v4, 0x7f, v0
	v_lshlrev_b32_e32 v18, 4, v4
	v_mov_b32_e32 v19, 0
	v_lshl_add_u64 v[4:5], s[14:15], 0, v[18:19]
	s_mov_b32 s2, 0x37000
	v_add_co_u32_e64 v4, s[2:3], s2, v4
	s_nop 1
	v_addc_co_u32_e64 v5, s[2:3], 0, v5, s[2:3]
	global_load_dwordx4 v[14:17], v[4:5], off offset:2112
	s_movk_i32 s22, 0x410
	s_movk_i32 s2, 0x4ff
	v_and_b32_e32 v4, 63, v0
	v_cmp_lt_u32_e64 s[2:3], s2, v3
	s_mul_i32 s5, s7, 0x6000
	s_mul_hi_u32 s4, s7, 0x6000
	s_add_u32 s8, s14, s5
	s_addc_u32 s9, s15, s4
	v_lshlrev_b32_e32 v210, 4, v4
	v_mov_b32_e32 v211, v19
	v_lshl_add_u64 v[20:21], s[8:9], 0, v[210:211]
	s_movk_i32 s4, 0x2000
	v_add_co_u32_e64 v22, s[4:5], s4, v20
	s_nop 1
	v_addc_co_u32_e64 v23, s[4:5], 0, v21, s[4:5]
	s_movk_i32 s4, 0x3000
	s_nop 0
	v_add_co_u32_e64 v24, s[4:5], s4, v20
	global_load_dwordx4 v[90:93], v[22:23], off offset:1024
	global_load_dwordx4 v[86:89], v[22:23], off offset:2048
	v_addc_co_u32_e64 v25, s[4:5], 0, v21, s[4:5]
	s_movk_i32 s4, 0x5000
	s_nop 0
	v_add_co_u32_e64 v26, s[4:5], s4, v20
	s_nop 1
	v_addc_co_u32_e64 v27, s[4:5], 0, v21, s[4:5]
	global_load_dwordx4 v[82:85], v[22:23], off offset:3072
	global_load_dwordx4 v[46:49], v[26:27], off
	global_load_dwordx4 v[42:45], v[26:27], off offset:1024
	global_load_dwordx4 v[38:41], v[26:27], off offset:2048
	global_load_dwordx4 v[94:97], v[24:25], off offset:-4096
	global_load_dwordx4 v[34:37], v[26:27], off offset:3072
	s_movk_i32 s4, 0x1000
	v_add_co_u32_e64 v22, s[4:5], s4, v20
	global_load_dwordx4 v[126:129], v210, s[8:9]
	global_load_dwordx4 v[122:125], v210, s[8:9] offset:1024
	global_load_dwordx4 v[118:121], v210, s[8:9] offset:2048
	global_load_dwordx4 v[114:117], v210, s[8:9] offset:3072
	v_addc_co_u32_e64 v23, s[4:5], 0, v21, s[4:5]
	global_load_dwordx4 v[110:113], v[22:23], off
	global_load_dwordx4 v[106:109], v[22:23], off offset:1024
	global_load_dwordx4 v[102:105], v[22:23], off offset:2048
	global_load_dwordx4 v[98:101], v[22:23], off offset:3072
	global_load_dwordx4 v[78:81], v[24:25], off
	global_load_dwordx4 v[74:77], v[24:25], off offset:1024
	global_load_dwordx4 v[70:73], v[24:25], off offset:2048
	global_load_dwordx4 v[66:69], v[24:25], off offset:3072
	s_movk_i32 s4, 0x4000
	v_add_co_u32_e64 v20, s[4:5], s4, v20
	v_mov_b32_e32 v5, 0x4000
	s_nop 0
	v_addc_co_u32_e64 v21, s[4:5], 0, v21, s[4:5]
	global_load_dwordx4 v[62:65], v[20:21], off
	global_load_dwordx4 v[58:61], v[20:21], off offset:1024
	global_load_dwordx4 v[54:57], v[20:21], off offset:2048
	global_load_dwordx4 v[50:53], v[20:21], off offset:3072
	s_waitcnt vmcnt(26)
	ds_write_b128 v31, v[6:9] offset:16384
	v_lshl_or_b32 v5, v28, 4, v5
	v_add_u32_e32 v6, 0x9840, v31
	v_cndmask_b32_e32 v5, v6, v5, vcc
	s_waitcnt vmcnt(25)
	ds_write_b128 v5, v[10:13]
	s_waitcnt vmcnt(24)
	ds_write_b128 v18, v[14:17] offset:36928
	v_mul_u32_u24_e32 v5, 0xccd, v0
	v_lshrrev_b32_e32 v5, 16, v5
	s_mov_b32 s5, 0xffffec
	v_mul_u32_u24_e32 v6, 0xccd, v28
	s_movk_i32 s4, 0x90
	v_mad_u32_u24 v8, v5, s5, v0
	v_lshlrev_b32_e32 v5, 2, v5
	v_lshrrev_b32_e32 v6, 16, v6
	v_mul_lo_u32 v7, v29, s4
	v_lshl_or_b32 v5, v8, 8, v5
	ds_write_b32 v5, v7 offset:30784
	v_mul_lo_u32 v196, v29, s22
	v_add_u32_e32 v197, 0x24e80, v5
	ds_write_b32 v197, v196
	v_mad_u32_u24 v7, v6, s5, v28
	v_lshlrev_b32_e32 v6, 2, v6
	v_mul_lo_u32 v5, v30, s4
	v_lshl_or_b32 v6, v7, 8, v6
	ds_write_b32 v6, v5 offset:30784
	v_mul_lo_u32 v198, v30, s22
	v_add_u32_e32 v199, 0x24e80, v6
	ds_write_b32 v199, v198
	s_and_saveexec_b64 s[4:5], s[2:3]
	s_xor_b64 s[2:3], exec, s[4:5]
	v_mov_b32_e32 v3, 0x9840
	v_lshl_add_u32 v5, v0, 2, v3
	s_andn2_saveexec_b64 s[2:3], s[2:3]
	v_mul_u32_u24_e32 v5, 0xccd, v3
	s_mov_b32 s4, 0xffffec
	v_mul_u32_u24_sdwa v6, v5, s4 dst_sel:DWORD dst_unused:UNUSED_PAD src0_sel:WORD_1 src1_sel:DWORD
	v_add_lshl_u32 v3, v6, v3, 8
	v_mov_b32_e32 v6, 2
	v_lshlrev_b32_sdwa v5, v6, v5 dst_sel:DWORD dst_unused:UNUSED_PAD src0_sel:DWORD src1_sel:WORD_1
	s_movk_i32 s4, 0x7840
	v_add3_u32 v5, v5, v3, s4
	s_or_b64 exec, exec, s[2:3]
	v_lshrrev_b32_e32 v3, 5, v4
	s_movk_i32 s2, 0x90
	s_lshl_b32 s6, s7, 10
	s_mulk_i32 s7, 0xfd00
	v_and_b32_e32 v182, 31, v0
	v_mul_lo_u32 v200, v2, s22
	v_mul_lo_u32 v2, v2, s2
	s_add_i32 s7, s6, s7
	v_lshlrev_b32_e32 v229, 6, v3
	ds_write_b32 v5, v2
	v_add_u32_e32 v201, 0x1d640, v5
	ds_write_b32 v201, v200
	v_lshlrev_b32_e32 v230, 4, v3
	v_lshlrev_b32_e32 v228, 2, v182
	v_or_b32_e32 v2, s7, v229
	v_mov_b32_e32 v204, 0
	v_mov_b32_e32 v205, 0
	v_mov_b32_e32 v206, 0
	v_mov_b32_e32 v207, 0
	ds_write_b128 v31, v[204:207]
	ds_write_b128 v31, v[204:207] offset:8192
	v_and_b32_e32 v202, 0xfc, v1
	v_add_u32_e32 v202, 0x26280, v202
	ds_write_b32 v202, v204
	s_waitcnt lgkmcnt(0)
	s_barrier
	s_cmpk_lt_u32 s19, 0x100
	s_cbranch_scc1 .Llight_path
	s_setprio 1
	s_nop 0
	v_add_u32_e32 v3, 0x7800, v228
	ds_read2_b32 v[138:139], v3 offset0:16 offset1:48
	ds_read_b128 v[18:21], v2 offset:36928
	ds_read_b128 v[22:25], v2 offset:36944
	s_waitcnt lgkmcnt(2)
	v_add_u32_e32 v3, v230, v138
	ds_read_b128 v[26:29], v2 offset:36960
	ds_read_b128 v[30:33], v2 offset:36976
	ds_read_b128 v[142:145], v3 offset:16384
	ds_read_b128 v[130:133], v3 offset:16416
	ds_read_b128 v[154:157], v3 offset:16448
	ds_read_b128 v[134:137], v3 offset:16480
	ds_read_b128 v[248:251], v2 offset:37104
	ds_read_b128 v[244:247], v2 offset:37088
	ds_read_b128 v[240:243], v2 offset:37072
	ds_read_b128 v[236:239], v2 offset:37056
	s_waitcnt vmcnt(17) lgkmcnt(7)
	v_mfma_f32_32x32x16_bf16 v[18:33], v[94:97], v[142:145], v[18:33]
	s_waitcnt lgkmcnt(6)
	v_mfma_f32_32x32x16_bf16 v[18:33], v[90:93], v[130:133], v[18:33]
	s_waitcnt lgkmcnt(5)
	v_mfma_f32_32x32x16_bf16 v[18:33], v[86:89], v[154:157], v[18:33]
	s_waitcnt lgkmcnt(4)
	v_mfma_f32_32x32x16_bf16 v[18:33], v[82:85], v[134:137], v[18:33]
	s_cmpk_lt_u32 s19, 0x100
	s_cselect_b64 s[2:3], -1, 0
	ds_read_b32 v158, v228 offset:31040
	v_add_u32_e32 v159, v230, v139
	s_nop 2
	v_exp_f32_e32 v139, v20
	v_exp_f32_e32 v138, v24
	v_exp_f32_e32 v141, v28
	v_exp_f32_e32 v140, v32
	v_exp_f32_e32 v18, v18
	v_exp_f32_e32 v20, v22
	v_exp_f32_e32 v22, v26
	v_add_f32_e32 v24, 1.0, v138
	v_add_f32_e32 v26, 1.0, v141
	v_add_f32_e32 v19, 1.0, v139
	v_exp_f32_e32 v23, v30
	v_add_f32_e32 v27, 1.0, v140
	v_fmac_f32_e32 v24, v20, v24
	v_fmac_f32_e32 v26, v22, v26
	v_fmac_f32_e32 v19, v18, v19
	v_fmac_f32_e32 v27, v23, v27
	v_rcp_f32_e32 v18, v24
	v_rcp_f32_e32 v22, v27
	v_rcp_f32_e32 v19, v19
	v_rcp_f32_e32 v23, v26
	v_exp_f32_e32 v146, v21
	v_exp_f32_e32 v147, v25
	s_mov_b32 s8, 0xc038aa3b
	s_mov_b32 s4, 0x4038aa3b
	v_mov_b64_e32 v[160:161], s[8:9]
	v_exp_f32_e32 v148, v29
	v_exp_f32_e32 v149, v33
	v_pk_fma_f32 v[20:21], v[138:139], s[4:5], v[160:161] op_sel_hi:[1,0,0]
	s_nop 0
	v_pk_mul_f32 v[214:215], v[20:21], v[18:19]
	v_pk_fma_f32 v[18:19], v[140:141], s[4:5], v[160:161] op_sel_hi:[1,0,0]
	s_nop 0
	v_pk_mul_f32 v[212:213], v[18:19], v[22:23]
	v_add_u32_e32 v231, s7, v229
	ds_read_b128 v[18:21], v231 offset:36928
	ds_read_b128 v[22:25], v231 offset:36944
	ds_read_b128 v[26:29], v231 offset:36960
	ds_read_b128 v[30:33], v231 offset:36976
	s_waitcnt lgkmcnt(5)
	v_mfma_f32_32x32x16_bf16 v[2:17], v[46:49], v[142:145], v[236:251]
	ds_read_b128 v[138:141], v159 offset:16384
	v_add_f32_e32 v162, 1.0, v146
	v_exp_f32_e32 v163, v215
	v_exp_f32_e32 v164, v214
	v_exp_f32_e32 v165, v213
	v_exp_f32_e32 v166, v212
	v_add_f32_e32 v142, 1.0, v147
	v_add_f32_e32 v143, 1.0, v148
	v_add_f32_e32 v144, 1.0, v149
	v_mfma_f32_32x32x16_bf16 v[2:17], v[42:45], v[130:133], v[2:17]
	ds_read_b128 v[146:149], v159 offset:16416
	v_fmac_f32_e32 v162, v162, v163
	v_fmac_f32_e32 v142, v142, v164
	v_fmac_f32_e32 v143, v143, v165
	v_fmac_f32_e32 v144, v144, v166
	v_mfma_f32_32x32x16_bf16 v[2:17], v[38:41], v[154:157], v[2:17]
	ds_read_b128 v[150:153], v159 offset:16448
	v_rcp_f32_e32 v130, v162
	v_rcp_f32_e32 v131, v142
	v_rcp_f32_e32 v132, v143
	v_rcp_f32_e32 v133, v144
	s_waitcnt vmcnt(16)
	v_mfma_f32_32x32x16_bf16 v[2:17], v[34:37], v[134:137], v[2:17]
	ds_read_b128 v[178:181], v159 offset:16480
	v_fma_f32 v130, -v163, v130, v130
	v_fma_f32 v131, -v164, v131, v131
	v_fma_f32 v132, -v165, v132, v132
	v_fma_f32 v133, -v166, v133, v133
	v_add_u32_e32 v211, s6, v210
	v_cvt_pk_bf16_f32 v130, v130, v131
	v_cvt_pk_bf16_f32 v131, v132, v133
	ds_write_b64 v211, v[130:131]
	s_nop 3
	v_exp_f32_e32 v131, v4
	v_exp_f32_e32 v130, v8
	v_exp_f32_e32 v133, v12
	v_exp_f32_e32 v132, v16
	v_exp_f32_e32 v2, v2
	v_exp_f32_e32 v4, v6
	v_exp_f32_e32 v6, v10
	v_exp_f32_e32 v7, v14
	v_add_f32_e32 v3, 1.0, v131
	v_add_f32_e32 v8, 1.0, v130
	v_add_f32_e32 v10, 1.0, v133
	v_add_f32_e32 v11, 1.0, v132
	v_fmac_f32_e32 v3, v2, v3
	v_fmac_f32_e32 v8, v4, v8
	v_fmac_f32_e32 v10, v6, v10
	v_fmac_f32_e32 v11, v7, v11
	v_rcp_f32_e32 v3, v3
	v_rcp_f32_e32 v2, v8
	v_rcp_f32_e32 v7, v10
	v_rcp_f32_e32 v6, v11
	v_exp_f32_e32 v134, v5
	v_exp_f32_e32 v135, v9
	v_pk_fma_f32 v[4:5], v[130:131], s[4:5], v[160:161] op_sel_hi:[1,0,0]
	v_exp_f32_e32 v130, v13
	v_pk_mul_f32 v[204:205], v[4:5], v[2:3]
	v_pk_fma_f32 v[2:3], v[132:133], s[4:5], v[160:161] op_sel_hi:[1,0,0]
	v_exp_f32_e32 v131, v17
	v_pk_mul_f32 v[202:203], v[2:3], v[6:7]
	s_waitcnt lgkmcnt(4)
	v_mfma_f32_32x32x16_bf16 v[18:33], v[94:97], v[138:141], v[18:33]
	v_add_f32_e32 v132, 1.0, v134
	v_exp_f32_e32 v133, v205
	v_add_f32_e32 v134, 1.0, v135
	v_exp_f32_e32 v135, v204
	v_exp_f32_e32 v136, v203
	v_exp_f32_e32 v137, v202
	v_add_f32_e32 v130, 1.0, v130
	v_add_f32_e32 v131, 1.0, v131
	s_waitcnt lgkmcnt(3)
	v_mfma_f32_32x32x16_bf16 v[18:33], v[90:93], v[146:149], v[18:33]
	v_fmac_f32_e32 v132, v132, v133
	v_fmac_f32_e32 v134, v134, v135
	v_fmac_f32_e32 v130, v130, v136
	v_fmac_f32_e32 v131, v131, v137
	s_waitcnt lgkmcnt(2)
	v_mfma_f32_32x32x16_bf16 v[18:33], v[86:89], v[150:153], v[18:33]
	v_rcp_f32_e32 v132, v132
	v_rcp_f32_e32 v134, v134
	v_rcp_f32_e32 v130, v130
	v_rcp_f32_e32 v131, v131
	s_waitcnt lgkmcnt(1)
	v_mfma_f32_32x32x16_bf16 v[18:33], v[82:85], v[178:181], v[18:33]
	v_fma_f32 v132, -v133, v132, v132
	v_fma_f32 v133, -v135, v134, v134
	v_fma_f32 v134, -v136, v130, v130
	v_fma_f32 v131, -v137, v131, v131
	v_cvt_pk_bf16_f32 v130, v132, v133
	v_cvt_pk_bf16_f32 v131, v134, v131
	ds_write_b64 v211, v[130:131] offset:8
	s_waitcnt lgkmcnt(0)
	s_barrier
	s_load_dwordx8 s[4:11], s[0:1], 0x10
	ds_read_b32 v194, v228 offset:31168
	ds_read_b128 v[174:177], v210
	v_add_u32_e32 v183, v230, v158
	ds_read_b128 v[170:173], v210 offset:1024
	v_exp_f32_e32 v131, v20
	v_exp_f32_e32 v130, v24
	v_exp_f32_e32 v133, v28
	v_exp_f32_e32 v132, v32
	ds_read_b128 v[166:169], v210 offset:2048
	v_exp_f32_e32 v18, v18
	v_exp_f32_e32 v20, v22
	v_exp_f32_e32 v22, v26
	v_exp_f32_e32 v23, v30
	v_add_f32_e32 v19, 1.0, v131
	v_add_f32_e32 v24, 1.0, v130
	v_add_f32_e32 v26, 1.0, v133
	v_add_f32_e32 v27, 1.0, v132
	ds_read_b128 v[162:165], v210 offset:3072
	v_fmac_f32_e32 v19, v18, v19
	v_fmac_f32_e32 v24, v20, v24
	v_fmac_f32_e32 v26, v22, v26
	v_fmac_f32_e32 v27, v23, v27
	ds_read_b128 v[158:161], v210 offset:4096
	v_rcp_f32_e32 v19, v19
	v_rcp_f32_e32 v18, v24
	v_rcp_f32_e32 v23, v26
	v_rcp_f32_e32 v22, v27
	ds_read_b128 v[154:157], v210 offset:5120
	v_exp_f32_e32 v186, v21
	v_exp_f32_e32 v187, v25
	ds_read_b128 v[142:145], v210 offset:6144
	s_mov_b32 s0, 0xc038aa3b
	s_mov_b32 s12, 0x4038aa3b
	v_mov_b64_e32 v[184:185], s[0:1]
	v_pk_fma_f32 v[20:21], v[130:131], s[12:13], v[184:185] op_sel_hi:[1,0,0]
	v_exp_f32_e32 v188, v29
	v_pk_mul_f32 v[200:201], v[20:21], v[18:19]
	v_pk_fma_f32 v[18:19], v[132:133], s[12:13], v[184:185] op_sel_hi:[1,0,0]
	v_exp_f32_e32 v189, v33
	v_pk_mul_f32 v[198:199], v[18:19], v[22:23]
	ds_read_b128 v[130:133], v210 offset:7168
	ds_read_b128 v[18:21], v231 offset:36928
	ds_read_b128 v[22:25], v231 offset:36944
	ds_read_b128 v[26:29], v231 offset:36960
	ds_read_b128 v[30:33], v231 offset:36976
	v_mfma_f32_32x32x16_bf16 v[2:17], v[46:49], v[138:141], v[236:251]
	ds_read_b128 v[134:137], v183 offset:16384
	v_add_f32_e32 v186, 1.0, v186
	v_exp_f32_e32 v190, v201
	v_exp_f32_e32 v191, v200
	v_exp_f32_e32 v192, v199
	v_exp_f32_e32 v193, v198
	v_add_f32_e32 v187, 1.0, v187
	v_add_f32_e32 v188, 1.0, v188
	v_add_f32_e32 v189, 1.0, v189
	v_mfma_f32_32x32x16_bf16 v[2:17], v[42:45], v[146:149], v[2:17]
	ds_read_b128 v[138:141], v183 offset:16416
	v_fmac_f32_e32 v186, v186, v190
	v_fmac_f32_e32 v187, v187, v191
	v_fmac_f32_e32 v188, v188, v192
	v_fmac_f32_e32 v189, v189, v193
	v_mfma_f32_32x32x16_bf16 v[2:17], v[38:41], v[150:153], v[2:17]
	ds_read_b128 v[146:149], v183 offset:16448
	v_rcp_f32_e32 v186, v186
	v_rcp_f32_e32 v187, v187
	v_rcp_f32_e32 v188, v188
	v_rcp_f32_e32 v189, v189
	v_mfma_f32_32x32x16_bf16 v[2:17], v[34:37], v[178:181], v[2:17]
	ds_read_b128 v[150:153], v183 offset:16480
	v_fma_f32 v183, -v190, v186, v186
	v_fma_f32 v186, -v191, v187, v187
	v_fma_f32 v187, -v192, v188, v188
	v_fma_f32 v188, -v193, v189, v189
	s_waitcnt vmcnt(15) lgkmcnt(0)
	v_mfma_f32_32x32x16_bf16 v[18:33], v[126:129], v[174:177], v[18:33]
	v_cvt_pk_bf16_f32 v178, v183, v186
	v_cvt_pk_bf16_f32 v179, v187, v188
	ds_write_b64 v211, v[178:179] offset:8192
	s_waitcnt vmcnt(14)
	v_mfma_f32_32x32x16_bf16 v[18:33], v[122:125], v[170:173], v[18:33]
	s_nop 0
	v_exp_f32_e32 v179, v4
	v_exp_f32_e32 v178, v8
	v_exp_f32_e32 v181, v12
	v_exp_f32_e32 v180, v16
	s_waitcnt vmcnt(13)
	v_mfma_f32_32x32x16_bf16 v[18:33], v[118:121], v[166:169], v[18:33]
	v_exp_f32_e32 v2, v2
	v_exp_f32_e32 v4, v6
	v_exp_f32_e32 v7, v10
	v_exp_f32_e32 v8, v14
	v_add_f32_e32 v3, 1.0, v179
	v_add_f32_e32 v6, 1.0, v178
	v_add_f32_e32 v10, 1.0, v181
	v_add_f32_e32 v11, 1.0, v180
	s_waitcnt vmcnt(12)
	v_mfma_f32_32x32x16_bf16 v[18:33], v[114:117], v[162:165], v[18:33]
	v_fmac_f32_e32 v3, v2, v3
	v_fmac_f32_e32 v6, v4, v6
	v_fmac_f32_e32 v10, v7, v10
	v_fmac_f32_e32 v11, v8, v11
	s_waitcnt vmcnt(11)
	v_mfma_f32_32x32x16_bf16 v[18:33], v[110:113], v[158:161], v[18:33]
	v_rcp_f32_e32 v3, v3
	v_rcp_f32_e32 v2, v6
	v_rcp_f32_e32 v7, v10
	v_rcp_f32_e32 v6, v11
	s_waitcnt vmcnt(10)
	v_mfma_f32_32x32x16_bf16 v[18:33], v[106:109], v[154:157], v[18:33]
	v_exp_f32_e32 v183, v5
	v_exp_f32_e32 v186, v9
	s_waitcnt vmcnt(9)
	v_mfma_f32_32x32x16_bf16 v[18:33], v[102:105], v[142:145], v[18:33]
	v_fma_f32 v4, v178, s12, v184
	v_fma_f32 v5, v179, s12, v184
	v_exp_f32_e32 v178, v13
	v_pk_mul_f32 v[206:207], v[4:5], v[2:3]
	v_pk_fma_f32 v[2:3], v[180:181], s[12:13], v[184:185] op_sel_hi:[1,0,0]
	v_exp_f32_e32 v179, v17
	v_pk_mul_f32 v[208:209], v[2:3], v[6:7]
	s_waitcnt vmcnt(8)
	v_mfma_f32_32x32x16_bf16 v[18:33], v[98:101], v[130:133], v[18:33]
	v_mfma_f32_32x32x16_bf16 v[18:33], v[94:97], v[134:137], v[18:33]
	v_add_f32_e32 v180, 1.0, v183
	v_exp_f32_e32 v181, v207
	v_add_f32_e32 v183, 1.0, v186
	v_exp_f32_e32 v184, v206
	v_exp_f32_e32 v185, v209
	v_exp_f32_e32 v186, v208
	v_add_f32_e32 v178, 1.0, v178
	v_add_f32_e32 v179, 1.0, v179
	v_mfma_f32_32x32x16_bf16 v[18:33], v[90:93], v[138:141], v[18:33]
	v_fmac_f32_e32 v180, v180, v181
	v_fmac_f32_e32 v183, v183, v184
	v_fmac_f32_e32 v178, v178, v185
	v_fmac_f32_e32 v179, v179, v186
	v_mfma_f32_32x32x16_bf16 v[18:33], v[86:89], v[146:149], v[18:33]
	v_rcp_f32_e32 v180, v180
	v_rcp_f32_e32 v183, v183
	v_rcp_f32_e32 v178, v178
	v_rcp_f32_e32 v179, v179
	v_mfma_f32_32x32x16_bf16 v[18:33], v[82:85], v[150:153], v[18:33]
	v_fma_f32 v180, -v181, v180, v180
	v_fma_f32 v181, -v184, v183, v183
	v_fma_f32 v183, -v185, v178, v178
	v_fma_f32 v179, -v186, v179, v179
	v_cvt_pk_bf16_f32 v178, v180, v181
	v_cvt_pk_bf16_f32 v179, v183, v179
	ds_write_b64 v211, v[178:179] offset:8200
	s_waitcnt lgkmcnt(0)
	s_barrier
	v_mov_b32_e32 v178, 0x7a40
	v_lshl_add_u32 v232, v182, 2, v178
	s_mov_b32 s1, -1
	s_branch .LBB1_14
